# code placement: L1 attention loop shifted +4 bytes (main-loop head now 0 mod 8, as in the baseline object); later code phase kept
# speedup vs baseline: 1.0122x; 1.0122x over previous
.LBB0_872:
	s_add_i32 s21, s21, 1
	s_cmp_eq_u32 s21, 4
	s_cbranch_scc1 .LBB0_962
	s_nop 0

.LBB0_959:
	v_max_f32_e32 v16, v16, v16
	v_max_f32_e32 v17, 0, v16
	v_exp_f32_e64 v16, -v17
	v_cmp_gt_u32_e32 vcc, 32, v230
	s_and_saveexec_b64 s[2:3], vcc
	ds_write_b32 v235, v16
	s_or_b64 exec, exec, s[2:3]
	v_sub_f32_e32 v113, v113, v17
	v_sub_f32_e32 v112, v112, v17
	v_sub_f32_e32 v111, v111, v17
	v_sub_f32_e32 v110, v110, v17
	v_sub_f32_e32 v109, v109, v17
	v_sub_f32_e32 v108, v108, v17
	v_sub_f32_e32 v107, v107, v17
	v_sub_f32_e32 v106, v106, v17
	v_sub_f32_e32 v105, v105, v17
	v_sub_f32_e32 v104, v104, v17
	v_sub_f32_e32 v103, v103, v17
	v_sub_f32_e32 v102, v102, v17
	v_sub_f32_e32 v101, v101, v17
	v_sub_f32_e32 v100, v100, v17
	v_sub_f32_e32 v99, v99, v17
	v_sub_f32_e32 v98, v98, v17
	v_sub_f32_e32 v97, v97, v17
	v_sub_f32_e32 v96, v96, v17
	v_sub_f32_e32 v95, v95, v17
	v_sub_f32_e32 v94, v94, v17
	v_sub_f32_e32 v93, v93, v17
	v_sub_f32_e32 v92, v92, v17
	v_sub_f32_e32 v91, v91, v17
	v_sub_f32_e32 v90, v90, v17
	v_sub_f32_e32 v89, v89, v17
	v_sub_f32_e32 v88, v88, v17
	v_sub_f32_e32 v87, v87, v17
	v_sub_f32_e32 v86, v86, v17
	v_sub_f32_e32 v85, v85, v17
	v_sub_f32_e32 v84, v84, v17
	v_sub_f32_e32 v83, v83, v17
	v_sub_f32_e32 v82, v82, v17
	v_mul_f32_e32 v243, v243, v16
	s_branch .LBB0_953
	s_nop 0
